# v62 plus phase-19 queue split per XCD (contiguous 32-block range each, own counter) with a static first ticket for the non-scan workgroups
# baseline (speedup 1.0000x reference)
; #define LAS __attribute__((address_space(3)))
; __global__ void __launch_bounds__(512, 2) fwd_kernel(Args args) {
;     ...
;                 {   unsigned* qh = (unsigned*)(ws + WS_QUE) + 16 * (layer * NBATCH + b);
;                     volatile LAS unsigned* qs = (volatile LAS unsigned*)(c.lds + LDS_MISC + 1024);
;                     unsigned nxt = 0u;
;                     if (c.tid == 0) nxt = __hip_atomic_fetch_add(qh, 1u, __ATOMIC_RELAXED, __HIP_MEMORY_SCOPE_AGENT);
;                     __syncthreads();
;                     ((LAS float*)(c.lds + ATTN_REL_01))[c.tid] = inptr(c, I_REL)[c.tid];
.LBB0_982:
	v_readlane_b32 s0, v254, 29
	s_lshl_b32 s0, s0, 4
	v_readlane_b32 s1, v254, 27
	s_or_b32 s42, s0, s1
	s_lshl_b64 s[0:1], s[42:43], 2
	v_readlane_b32 s2, v252, 29
	s_add_u32 s2, s2, s0
	v_readlane_b32 s0, v252, 30
	s_addc_u32 s3, s0, s1
	s_mul_i32 s0, s42, 28
	s_add_u32 s2, s2, s0
	s_addc_u32 s3, s3, 0
	v_readlane_b32 s0, v251, 0
	s_and_b32 s0, s0, 7
	s_lshl_b32 s0, s0, 6
	s_addk_i32 s0, 0x400
	s_add_u32 s2, s2, s0
	s_addc_u32 s3, s3, 0
	v_mov_b32_e32 v142, 0
	v_readfirstlane_b32 s8, v178
	v_cmp_eq_u32_e32 vcc, 0, v178
	s_and_saveexec_b64 s[0:1], vcc
	s_cbranch_execz .LBB0_986
	v_readlane_b32 s4, v251, 0
	s_cmp_lt_u32 s4, 32
	s_cbranch_scc1 .Lq19_dyn
	s_lshr_b32 s4, s4, 3
	s_sub_i32 s4, s4, 32
	v_mov_b32_e32 v142, s4
	s_branch .LBB0_986
.Lq19_dyn:
	v_mov_b32_e32 v2, 1
	global_atomic_add v142, v1, v2, s[2:3] sc0
	s_waitcnt vmcnt(0)
.LBB0_986:
	s_or_b64 exec, exec, s[0:1]
	v_mov_b32_e32 v188, v142
	v_readlane_b32 s0, v253, 24
	s_waitcnt vmcnt(0) lgkmcnt(0)
	s_barrier
	v_mov_b32_e32 v0, s0
	ds_read_b32 v0, v0
	v_readlane_b32 s1, v253, 25
	v_ashrrev_i32_e32 v179, 31, v178
	v_and_b32_e32 v132, 63, v178
	s_ashr_i32 s20, s8, 6
	s_waitcnt lgkmcnt(0)
	v_readfirstlane_b32 s0, v0
	v_mov_b32_e32 v0, s1
	ds_read_b32 v0, v0
	v_mov_b32_e32 v2, s0
	v_mov_b32_e32 v234, 0x358637bd
	s_waitcnt lgkmcnt(0)
	v_readfirstlane_b32 s1, v0
	s_nop 1
	v_mov_b32_e32 v3, s1
	v_lshl_add_u64 v[2:3], v[178:179], 2, v[2:3]
	flat_load_dword v0, v[2:3]
	v_lshl_add_u32 v2, v178, 2, 0
	v_add_u32_e32 v2, 0x25500, v2
	s_waitcnt vmcnt(0) lgkmcnt(0)
	ds_write_b32 v2, v0
	s_branch .LBB0_989

; __global__ void __launch_bounds__(512, 2) fwd_kernel(Args args) {
;     ...
;                     for (;;) {
;                         __syncthreads();
;                         if (c.tid == 0) qs[0] = nxt;
;                         __syncthreads();
;                         const int u = __builtin_amdgcn_readfirstlane((int)qs[0]);
;                         if (u >= 1024) break;
;                         if (c.tid == 0) nxt = __hip_atomic_fetch_add(qh, 1u, __ATOMIC_RELAXED, __HIP_MEMORY_SCOPE_AGENT);
;                         if (u < 512) phase_attn<1, 2>(c, args, layer, proj, vtb, kcb, vctb, sel, nsaacc, obuf + (size_t)T * 512, u, false);
.LBB0_989:
	v_cmp_eq_u32_e64 s[0:1], 0, v178
	s_waitcnt lgkmcnt(0)
	s_barrier
	s_and_saveexec_b64 s[4:5], s[0:1]
	s_cbranch_execz .LBB0_991
	v_readlane_b32 s6, v253, 27
	s_nop 1
	v_mov_b32_e32 v0, s6
	s_waitcnt vmcnt(8)
	v_add_u32_e32 v188, 28, v188
	ds_write_b32 v0, v188
.LBB0_991:
	s_or_b64 exec, exec, s[4:5]
	v_readlane_b32 s4, v253, 27
	s_waitcnt lgkmcnt(0)
	s_barrier
	v_mov_b32_e32 v0, s4
	ds_read_b32 v0, v0
	s_waitcnt lgkmcnt(0)
	v_readfirstlane_b32 s21, v0
	v_readlane_b32 s12, v251, 0
	s_and_b32 s11, s21, 31
	s_and_b32 s12, s12, 7
	s_lshl_b32 s12, s12, 5
	s_add_i32 s11, s11, s12
	s_sub_i32 s12, 0x1ff, s11
	s_bitcmp1_b32 s21, 5
	s_cselect_b32 s11, s12, s11
	s_lshr_b32 s12, s21, 6
	s_lshl_b32 s12, s12, 9
	s_add_i32 s21, s11, s12
	s_cmpk_gt_i32 s21, 0x3ff
	s_cselect_b64 s[4:5], -1, 0
	s_and_b64 vcc, exec, s[4:5]
	s_cbranch_vccnz .LBB0_988
	s_and_saveexec_b64 s[6:7], s[0:1]
	s_cbranch_execnz .LBB0_995
	s_or_b64 exec, exec, s[6:7]
	s_cmpk_gt_i32 s21, 0x1ff
	s_mov_b64 s[0:1], -1
	s_cbranch_scc1 .LBB0_998

; __global__ void __launch_bounds__(512, 2) fwd_kernel(Args args) {
;     ...
;                         if (c.tid == 0) nxt = __hip_atomic_fetch_add(qh, 1u, __ATOMIC_RELAXED, __HIP_MEMORY_SCOPE_AGENT);
.LBB0_995:
	v_mov_b32_e32 v2, 1
	global_atomic_add v188, v1, v2, s[2:3] sc0
	s_or_b64 exec, exec, s[6:7]
	s_cmpk_gt_i32 s21, 0x1ff
	s_mov_b64 s[0:1], -1
	s_cbranch_scc0 .LBB0_994
